# speedup vs baseline: 1.0066x; 1.0029x over previous
.LBB1_15:
	s_or_b64 exec, exec, s[12:13]
	v_and_b32_e32 v114, 31, v0
	s_mul_i32 s9, s67, 0x60
	s_cmp_lg_u32 s67, 0
	s_cselect_b64 s[74:75], -1, 0
	v_alignbit_b32 v126, v113, v112, 24
	v_cndmask_b32_e64 v126, v112, v126, s[74:75]
	v_bfe_u32 v91, v126, 0, 8
	v_mul_lo_u16_e32 v15, 0x4f, v91
	s_lshl_b32 s7, s66, 3
	v_lshrrev_b16_e32 v15, 9, v15
	s_or_b32 s8, s7, 0xb600
	v_and_b32_e32 v15, 62, v15
	v_add_u32_e32 v15, v91, v15
	s_movk_i32 s6, 0x48
	v_mov_b32_e32 v99, s8
	v_mad_u32_u24 v42, v15, s6, v99
	v_mad_u32_u24 v43, v115, s6, v42
	s_waitcnt lgkmcnt(0)
	s_barrier
	ds_read_b64 v[34:35], v43
	ds_read_b64 v[36:37], v43 offset:8
	ds_read_b64 v[38:39], v43 offset:1080
	ds_read_b64 v[40:41], v43 offset:1088
	v_mov_b32_e32 v2, v46
	v_mov_b32_e32 v3, v46
	v_mov_b32_e32 v4, v46
	v_mov_b32_e32 v5, v46
	v_mov_b32_e32 v6, v47
	v_mov_b32_e32 v7, v47
	v_mov_b32_e32 v8, v47
	v_mov_b32_e32 v9, v47
	v_mov_b32_e32 v10, v48
	v_mov_b32_e32 v11, v48
	v_mov_b32_e32 v12, v48
	v_mov_b32_e32 v13, v48
	v_mov_b32_e32 v14, v49
	v_mov_b32_e32 v15, v49
	v_mov_b32_e32 v16, v49
	v_mov_b32_e32 v17, v49
	s_movk_i32 s8, 0x438
	s_add_i32 s12, s9, 32
	s_waitcnt lgkmcnt(2)
	v_mfma_f32_32x32x16_f16 v[18:33], v[86:89], v[34:37], v[2:17]
	v_add_u32_e32 v34, 0x8b8, v43
	ds_read_b64 v[36:37], v34 offset:8
	ds_read_b64 v[34:35], v34
	v_and_or_b32 v107, v0, 32, s7
	s_movk_i32 s7, 0x110
	v_mad_u32_u24 v91, v91, s7, v107
	s_add_i32 s9, s9, 64
	s_lshr_b32 s42, s3, 6
	s_waitcnt lgkmcnt(2)
	v_mfma_f32_32x32x16_f16 v[18:33], v[62:65], v[38:41], v[18:33]
	v_mad_u32_u24 v38, v115, s8, v42
	ds_read_b64 v[40:41], v38 offset:152
	ds_read_b64 v[38:39], v38 offset:144
	s_cmpk_lt_u32 s3, 0x100
	s_cselect_b64 s[30:31], -1, 0
	s_add_i32 s13, s69, 0x600
	s_add_i32 s14, s69, 0x700
	v_lshlrev_b32_e32 v116, 4, v115
	s_waitcnt lgkmcnt(2)
	v_mfma_f32_32x32x16_f16 v[18:33], v[58:61], v[34:37], v[18:33]
	v_add_u32_e32 v34, 0x870, v43
	ds_read_b64 v[36:37], v34 offset:8
	ds_read_b64 v[34:35], v34
	s_movk_i32 s15, 0x1070
	s_movk_i32 s16, 0x1ba0
	s_movk_i32 s17, 0x1c20
	s_waitcnt lgkmcnt(2)
	v_mfma_f32_32x32x16_f16 v[18:33], v[54:57], v[38:41], v[18:33]
	v_bfe_u32 v101, v126, 8, 8
	v_mul_lo_u16_e32 v38, 0x4f, v101
	v_lshrrev_b16_e32 v38, 9, v38
	v_and_b32_e32 v38, 62, v38
	v_add_u32_e32 v38, v101, v38
	v_mad_u32_u24 v97, v38, s6, v99
	v_mad_u32_u24 v106, v115, s6, v97
	ds_read_b64 v[92:93], v106
	ds_read_b64 v[94:95], v106 offset:8
	v_add_u32_e32 v96, 0x8b8, v106
	ds_read_b64 v[102:103], v96
	ds_read_b64 v[104:105], v96 offset:8
	s_waitcnt lgkmcnt(4)
	v_mfma_f32_32x32x16_f16 v[18:33], v[50:53], v[34:37], v[18:33]
	s_add_i32 s12, s69, 0x500
	s_addk_i32 s69, 0x800
	s_cmpk_gt_u32 s3, 0xff
	s_cselect_b64 vcc, -1, 0
	s_waitcnt lgkmcnt(2)
	v_mfma_f32_32x32x16_f16 v[34:49], v[86:89], v[92:95], v[2:17]
	ds_read_b64 v[92:93], v106 offset:1080
	ds_read_b64 v[94:95], v106 offset:1088
	s_nop 4
	v_cvt_pk_f16_f32 v18, v18, v19
	v_pk_max_f16 v96, v18, 0
	v_mad_u32_u24 v18, v115, s8, v97
	v_cvt_pk_f16_f32 v22, v22, v23
	v_add_u32_e32 v23, 0x870, v106
	v_cvt_pk_f16_f32 v30, v30, v31
	s_waitcnt lgkmcnt(0)
	v_mfma_f32_32x32x16_f16 v[34:49], v[62:65], v[92:95], v[34:49]
	v_cvt_pk_f16_f32 v92, v20, v21
	ds_read_b64 v[20:21], v18 offset:152
	ds_read_b64 v[18:19], v18 offset:144
	v_pk_max_f16 v97, v92, 0
	ds_read_b64 v[92:93], v23
	ds_read_b64 v[94:95], v23 offset:8
	v_cvt_pk_f16_f32 v31, v32, v33
	v_mfma_f32_32x32x16_f16 v[34:49], v[58:61], v[102:105], v[34:49]
	v_or_b32_e32 v102, 64, v114
	s_waitcnt lgkmcnt(2)
	v_mfma_f32_32x32x16_f16 v[34:49], v[54:57], v[18:21], v[34:49]
	v_cvt_pk_f16_f32 v19, v24, v25
	v_pk_max_f16 v18, v22, 0
	v_pk_max_f16 v19, v19, 0
	ds_write2_b64 v91, v[96:97], v[18:19] offset1:8
	v_cvt_pk_f16_f32 v18, v26, v27
	v_pk_max_f16 v26, v18, 0
	v_cvt_pk_f16_f32 v22, v28, v29
	v_bfe_u32 v28, v126, 16, 8
	v_mul_lo_u16_e32 v18, 0x4f, v28
	v_lshrrev_b16_e32 v18, 9, v18
	v_and_b32_e32 v18, 62, v18
	v_add_u32_e32 v18, v28, v18
	v_mad_u32_u24 v29, v18, s6, v99
	s_waitcnt lgkmcnt(1)
	v_mfma_f32_32x32x16_f16 v[34:49], v[50:53], v[92:95], v[34:49]
	v_add_u32_e32 v94, s68, v100
	v_add_u32_e32 v94, s69, v94
	v_mov_b32_e32 v95, 0
	v_lshl_add_u64 v[94:95], v[94:95], 4, s[22:23]
	global_load_dwordx4 v[94:97], v[94:95], off
	v_mad_u32_u24 v92, v115, s6, v29
	ds_read_b64 v[18:19], v92
	ds_read_b64 v[20:21], v92 offset:8
	v_pk_max_f16 v27, v22, 0
	ds_read_b64 v[22:23], v92 offset:1080
	ds_read_b64 v[24:25], v92 offset:1088
	v_or_b32_e32 v99, 32, v114
	s_nop 6
	v_cvt_pk_f16_f32 v32, v40, v41
	s_waitcnt lgkmcnt(2)
	v_mfma_f32_32x32x16_f16 v[2:17], v[86:89], v[18:21], v[2:17]
	v_pk_max_f16 v18, v30, 0
	v_pk_max_f16 v19, v31, 0
	ds_write2_b64 v91, v[26:27], v[18:19] offset0:16 offset1:24
	v_cvt_pk_f16_f32 v18, v34, v35
	v_cvt_pk_f16_f32 v19, v36, v37
	v_pk_max_f16 v26, v18, 0
	v_add_u32_e32 v18, 0x8b8, v92
	s_waitcnt lgkmcnt(1)
	v_mfma_f32_32x32x16_f16 v[2:17], v[62:65], v[22:25], v[2:17]
	v_pk_max_f16 v27, v19, 0
	ds_read_b64 v[20:21], v18 offset:8
	ds_read_b64 v[18:19], v18
	v_mad_u32_u24 v22, v115, s8, v29
	ds_read_b64 v[24:25], v22 offset:152
	ds_read_b64 v[22:23], v22 offset:144
	v_cvt_pk_f16_f32 v31, v38, v39
	v_mad_u32_u24 v30, v101, s7, v107
	s_and_b64 s[8:9], vcc, exec
	s_waitcnt lgkmcnt(2)
	v_mfma_f32_32x32x16_f16 v[2:17], v[58:61], v[18:21], v[2:17]
	v_pk_max_f16 v18, v31, 0
	v_pk_max_f16 v19, v32, 0
	ds_write2_b64 v30, v[26:27], v[18:19] offset1:8
	v_cvt_pk_f16_f32 v18, v42, v43
	v_cvt_pk_f16_f32 v19, v44, v45
	v_pk_max_f16 v26, v18, 0
	v_add_u32_e32 v18, 0x870, v92
	s_waitcnt lgkmcnt(1)
	v_mfma_f32_32x32x16_f16 v[2:17], v[54:57], v[22:25], v[2:17]
	v_pk_max_f16 v27, v19, 0
	ds_read_b64 v[20:21], v18 offset:8
	ds_read_b64 v[18:19], v18
	v_cvt_pk_f16_f32 v22, v46, v47
	v_cvt_pk_f16_f32 v23, v48, v49
	v_pk_max_f16 v22, v22, 0
	v_pk_max_f16 v23, v23, 0
	ds_write2_b64 v30, v[26:27], v[22:23] offset0:16 offset1:24
	s_waitcnt lgkmcnt(1)
	v_mfma_f32_32x32x16_f16 v[2:17], v[50:53], v[18:21], v[2:17]
	v_mad_u32_u24 v18, v28, s7, v107
	v_lshl_or_b32 v42, s66, 5, v116
	s_cselect_b32 s8, 0xf60, 0
	s_movk_i32 s9, 0xff0
	s_cselect_b32 s9, s9, 0x80
	s_cselect_b32 s15, s15, 0x110
	s_cselect_b32 s16, s16, 0x190
	s_nop 4
	v_cvt_pk_f16_f32 v2, v2, v3
	v_cvt_pk_f16_f32 v3, v4, v5
	v_cvt_pk_f16_f32 v4, v6, v7
	v_cvt_pk_f16_f32 v5, v8, v9
	v_pk_max_f16 v2, v2, 0
	v_pk_max_f16 v3, v3, 0
	v_pk_max_f16 v4, v4, 0
	v_pk_max_f16 v5, v5, 0
	ds_write2_b64 v18, v[2:3], v[4:5] offset1:8
	v_cvt_pk_f16_f32 v2, v10, v11
	v_cvt_pk_f16_f32 v3, v12, v13
	v_cvt_pk_f16_f32 v4, v14, v15
	v_cvt_pk_f16_f32 v5, v16, v17
	v_pk_max_f16 v2, v2, 0
	v_pk_max_f16 v3, v3, 0
	v_pk_max_f16 v4, v4, 0
	v_pk_max_f16 v5, v5, 0
	ds_write2_b64 v18, v[2:3], v[4:5] offset0:16 offset1:24
	s_waitcnt vmcnt(0)
	v_bfe_u32 v2, v117, 0, 8
	v_mul_u32_u24_e32 v3, 0xbb, v2
	v_lshrrev_b32_e32 v3, 11, v3
	v_lshl_add_u32 v103, v3, 1, v2
	v_bfe_u32 v2, v117, 8, 8
	v_mul_u32_u24_e32 v3, 0xbb, v2
	v_lshrrev_b32_e32 v3, 11, v3
	v_lshl_add_u32 v106, v3, 1, v2
	v_mad_u32_u24 v90, v103, s7, v42
	v_mad_u32_u24 v91, v106, s7, v42
	v_add_u32_e32 v2, s8, v90
	v_add_u32_e32 v6, s8, v91
	s_waitcnt lgkmcnt(0)
	s_barrier
	ds_read_b128 v[2:5], v2
	ds_read_b128 v[6:9], v6
	s_waitcnt lgkmcnt(1)
	v_mfma_f32_32x32x16_f16 v[18:33], v[82:85], v[2:5], 0
	v_add_u32_e32 v34, s9, v90
	v_add_u32_e32 v38, s9, v91
	ds_read_b128 v[34:37], v34
	ds_read_b128 v[38:41], v38
	s_cselect_b32 s17, s17, 0x220
	v_or_b32_e32 v101, 0x60, v114
	s_waitcnt lgkmcnt(2)
	v_mfma_f32_32x32x16_f16 v[2:17], v[82:85], v[6:9], 0
	s_waitcnt lgkmcnt(1)
	v_mfma_f32_32x32x16_f16 v[18:33], v[74:77], v[34:37], v[18:33]
	v_add_u32_e32 v34, s15, v90
	ds_read_b128 v[34:37], v34
	s_waitcnt lgkmcnt(1)
	v_mfma_f32_32x32x16_f16 v[2:17], v[74:77], v[38:41], v[2:17]
	v_add_u32_e32 v38, s15, v91
	ds_read_b128 v[38:41], v38
	s_waitcnt lgkmcnt(1)
	v_mfma_f32_32x32x16_f16 v[18:33], v[78:81], v[34:37], v[18:33]
	v_add_u32_e32 v34, s16, v90
	ds_read_b128 v[34:37], v34
	s_waitcnt lgkmcnt(1)
	v_mfma_f32_32x32x16_f16 v[2:17], v[78:81], v[38:41], v[2:17]
	v_add_u32_e32 v38, s16, v91
	ds_read_b128 v[38:41], v38
	s_waitcnt lgkmcnt(1)
	v_mfma_f32_32x32x16_f16 v[18:33], v[70:73], v[34:37], v[18:33]
	v_bfe_u32 v43, v117, 16, 8
	v_mul_u32_u24_e32 v34, 0xbb, v43
	v_lshrrev_b32_e32 v104, 11, v34
	v_add_u32_e32 v34, s17, v90
	ds_read_b128 v[34:37], v34
	v_lshl_add_u32 v104, v104, 1, v43
	v_mad_u32_u24 v92, v104, s7, v42
	s_waitcnt lgkmcnt(1)
	v_mfma_f32_32x32x16_f16 v[2:17], v[70:73], v[38:41], v[2:17]
	v_add_u32_e32 v38, s17, v91
	ds_read_b128 v[38:41], v38
	s_waitcnt lgkmcnt(1)
	v_mfma_f32_32x32x16_f16 v[18:33], v[66:69], v[34:37], v[18:33]
	v_bfe_u32 v34, v117, 24, 8
	v_mul_u32_u24_e32 v35, 0xbb, v34
	v_lshrrev_b32_e32 v35, 11, v35
	v_lshl_add_u32 v105, v35, 1, v34
	v_mad_u32_u24 v93, v105, s7, v42
	s_waitcnt lgkmcnt(0)
	v_mfma_f32_32x32x16_f16 v[2:17], v[66:69], v[38:41], v[2:17]
	v_add_u32_e32 v34, s8, v92
	v_add_u32_e32 v38, s8, v93
	ds_read_b128 v[34:37], v34
	ds_read_b128 v[38:41], v38
	v_add_u32_e32 v86, s9, v93
	s_waitcnt lgkmcnt(1)
	v_mfma_f32_32x32x16_f16 v[50:65], v[82:85], v[34:37], 0
	ds_read_b128 v[86:89], v86
	s_waitcnt lgkmcnt(1)
	v_mfma_f32_32x32x16_f16 v[34:49], v[82:85], v[38:41], 0
	v_add_u32_e32 v82, s9, v92
	ds_read_b128 v[82:85], v82
	s_waitcnt lgkmcnt(0)
	v_mfma_f32_32x32x16_f16 v[50:65], v[74:77], v[82:85], v[50:65]
	v_add_u32_e32 v82, s15, v93
	ds_read_b128 v[82:85], v82
	v_mfma_f32_32x32x16_f16 v[34:49], v[74:77], v[86:89], v[34:49]
	v_add_u32_e32 v74, s15, v92
	ds_read_b128 v[74:77], v74
	s_waitcnt lgkmcnt(0)
	v_mfma_f32_32x32x16_f16 v[50:65], v[78:81], v[74:77], v[50:65]
	v_add_u32_e32 v74, s16, v92
	ds_read_b128 v[74:77], v74
	v_mfma_f32_32x32x16_f16 v[34:49], v[78:81], v[82:85], v[34:49]
	v_add_u32_e32 v78, s16, v93
	ds_read_b128 v[78:81], v78
	s_waitcnt lgkmcnt(1)
	v_mfma_f32_32x32x16_f16 v[50:65], v[70:73], v[74:77], v[50:65]
	v_add_u32_e32 v74, s17, v93
	ds_read_b128 v[74:77], v74
	s_waitcnt lgkmcnt(1)
	v_mfma_f32_32x32x16_f16 v[34:49], v[70:73], v[78:81], v[34:49]
	v_add_u32_e32 v70, s17, v92
	ds_read_b128 v[70:73], v70
	s_waitcnt lgkmcnt(0)
	v_mfma_f32_32x32x16_f16 v[50:65], v[66:69], v[70:73], v[50:65]
	v_mfma_f32_32x32x16_f16 v[34:49], v[66:69], v[74:77], v[34:49]
	s_movk_i32 s7, 0x1cb0
	s_cselect_b32 s7, s7, 0x2a0
	v_add_u32_e32 v74, s7, v90
	ds_read_b128 v[74:77], v74
	v_add_u32_e32 v78, s7, v91
	ds_read_b128 v[78:81], v78
	s_movk_i32 s12, 0x1d30
	s_cselect_b32 s12, s12, 0xdd0
	s_movk_i32 s8, 0x1dc0
	s_cselect_b32 s8, s8, 0xe50
	s_movk_i32 s9, 0x1e40
	s_cselect_b32 s9, s9, 0xee0
	s_waitcnt vmcnt(0) lgkmcnt(1)
	v_mfma_f32_32x32x16_f16 v[18:33], v[108:111], v[74:77], v[18:33]
	v_add_u32_e32 v82, s12, v91
	ds_read_b128 v[82:85], v82
	s_waitcnt lgkmcnt(1)
	v_mfma_f32_32x32x16_f16 v[2:17], v[108:111], v[78:81], v[2:17]
	v_add_u32_e32 v78, s12, v90
	ds_read_b128 v[78:81], v78
	s_waitcnt lgkmcnt(0)
	v_mfma_f32_32x32x16_f16 v[18:33], v[118:121], v[78:81], v[18:33]
	v_add_u32_e32 v86, s8, v91
	ds_read_b128 v[86:89], v86
	v_mfma_f32_32x32x16_f16 v[2:17], v[118:121], v[82:85], v[2:17]
	v_add_u32_e32 v82, s8, v90
	ds_read_b128 v[82:85], v82
	s_waitcnt lgkmcnt(0)
	v_mfma_f32_32x32x16_f16 v[18:33], v[122:125], v[82:85], v[18:33]
	v_add_u32_e32 v82, s9, v90
	ds_read_b128 v[82:85], v82
	v_mfma_f32_32x32x16_f16 v[2:17], v[122:125], v[86:89], v[2:17]
	v_add_u32_e32 v86, s9, v91
	ds_read_b128 v[86:89], v86
	s_waitcnt lgkmcnt(1)
	v_mfma_f32_32x32x16_f16 v[18:33], v[94:97], v[82:85], v[18:33]
	s_waitcnt lgkmcnt(0)
	v_mfma_f32_32x32x16_f16 v[2:17], v[94:97], v[86:89], v[2:17]
	v_add_u32_e32 v82, s7, v92
	v_add_u32_e32 v86, s7, v93
	ds_read_b128 v[82:85], v82
	ds_read_b128 v[86:89], v86
	s_waitcnt lgkmcnt(1)
	v_mfma_f32_32x32x16_f16 v[50:65], v[108:111], v[82:85], v[50:65]
	v_add_u32_e32 v82, s12, v93
	ds_read_b128 v[82:85], v82
	s_waitcnt lgkmcnt(1)
	v_mfma_f32_32x32x16_f16 v[34:49], v[108:111], v[86:89], v[34:49]
	v_add_u32_e32 v66, s12, v92
	ds_read_b128 v[66:69], v66
	s_waitcnt lgkmcnt(0)
	v_mfma_f32_32x32x16_f16 v[50:65], v[118:121], v[66:69], v[50:65]
	v_add_u32_e32 v66, s8, v92
	ds_read_b128 v[66:69], v66
	v_mfma_f32_32x32x16_f16 v[34:49], v[118:121], v[82:85], v[34:49]
	v_add_u32_e32 v70, s8, v93
	ds_read_b128 v[70:73], v70
	s_waitcnt lgkmcnt(1)
	v_mfma_f32_32x32x16_f16 v[50:65], v[122:125], v[66:69], v[50:65]
	v_add_u32_e32 v66, s9, v92
	ds_read_b128 v[66:69], v66
	s_waitcnt lgkmcnt(1)
	v_mfma_f32_32x32x16_f16 v[34:49], v[122:125], v[70:73], v[34:49]
	v_add_u32_e32 v70, s9, v93
	ds_read_b128 v[70:73], v70
	s_waitcnt lgkmcnt(1)
	v_mfma_f32_32x32x16_f16 v[50:65], v[94:97], v[66:69], v[50:65]
	s_waitcnt lgkmcnt(0)
	v_mfma_f32_32x32x16_f16 v[34:49], v[94:97], v[70:73], v[34:49]
	s_cmpk_gt_u32 s3, 0x17f
	s_barrier
	s_cbranch_scc1 .LBB1_17
	s_mul_hi_u32 s7, s42, 0x55555556
	s_mul_i32 s7, s7, 3
	s_sub_i32 s7, s42, s7
	s_lshl_b32 s7, s7, 3
	s_add_i32 s8, s7, 0xb600
	s_cmpk_gt_u32 s3, 0xbf
	s_cselect_b64 s[74:75], -1, 0
	s_movk_i32 s12, 0x438
	s_movk_i32 s13, 0xd0
	v_alignbit_b32 v99, v113, v112, 24
	v_cndmask_b32_e64 v99, v112, v99, s[74:75]
	v_add_u32_e32 v122, 0xf550, v98
	ds_read_b128 v[82:85], v98 offset:62800
	ds_read_b128 v[86:89], v98 offset:63824
	ds_read_b128 v[90:93], v98 offset:64848
	ds_read_b128 v[94:97], v122 offset:3072
	ds_read_b128 v[118:121], v122 offset:4096
	ds_read_b32 v107, v122 offset:5120
	ds_read_b32 v112, v122 offset:5124
	ds_read_b32 v113, v122 offset:5128
	ds_read_b32 v117, v122 offset:5132
	v_bfe_u32 v101, v99, 0, 8
	v_mul_lo_u16_e32 v102, 0x4f, v101
	v_lshrrev_b16_e32 v102, 9, v102
	v_and_b32_e32 v102, 62, v102
	v_add_u32_e32 v102, v101, v102
	v_mov_b32_e32 v123, s8
	v_mad_u32_u24 v102, v102, s6, v123
	v_mad_u32_u24 v123, v115, s6, v102
	v_mad_u32_u24 v102, v115, s12, v102
	v_mad_u32_u24 v122, v115, 24, s7
	v_mad_u32_u24 v101, v101, s13, v122
	ds_read_b64 v[108:109], v123 offset:32
	ds_read_b64 v[110:111], v123 offset:40
	ds_read_b64 v[124:125], v123 offset:1112
	ds_read_b64 v[126:127], v123 offset:1120
	v_add_u32_e32 v122, 0x8d8, v123
	s_waitcnt lgkmcnt(2)
	v_mfma_f32_32x32x16_f16 v[66:81], v[82:85], v[108:111], 0
	ds_read_b64 v[108:109], v122
	ds_read_b64 v[110:111], v122 offset:8
	v_add_u32_e32 v122, 0x890, v123
	s_waitcnt lgkmcnt(2)
	v_mfma_f32_32x32x16_f16 v[66:81], v[86:89], v[124:127], v[66:81]
	ds_read_b64 v[124:125], v102 offset:176
	ds_read_b64 v[126:127], v102 offset:184
	s_waitcnt lgkmcnt(2)
	v_mfma_f32_32x32x16_f16 v[66:81], v[90:93], v[108:111], v[66:81]
	ds_read_b64 v[108:109], v122
	ds_read_b64 v[110:111], v122 offset:8
	s_waitcnt lgkmcnt(2)
	v_mfma_f32_32x32x16_f16 v[66:81], v[94:97], v[124:127], v[66:81]
	s_waitcnt lgkmcnt(0)
	v_mfma_f32_32x32x16_f16 v[66:81], v[118:121], v[108:111], v[66:81]
	v_bfe_u32 v124, v99, 8, 8
	v_mul_lo_u16_e32 v126, 0x4f, v124
	v_lshrrev_b16_e32 v126, 9, v126
	v_and_b32_e32 v126, 62, v126
	v_add_u32_e32 v126, v124, v126
	v_mov_b32_e32 v123, s8
	v_mad_u32_u24 v126, v126, s6, v123
	v_mad_u32_u24 v123, v115, s6, v126
	v_mad_u32_u24 v102, v115, s12, v126
	ds_read_b64 v[108:109], v123 offset:32
	ds_read_b64 v[110:111], v123 offset:40
	ds_read_b64 v[124:125], v123 offset:1112
	ds_read_b64 v[126:127], v123 offset:1120
	v_add_f32_e32 v66, v107, v66
	v_add_f32_e32 v67, v107, v67
	v_add_f32_e32 v68, v107, v68
	v_add_f32_e32 v69, v107, v69
	v_add_f32_e32 v70, v112, v70
	v_add_f32_e32 v71, v112, v71
	v_add_f32_e32 v72, v112, v72
	v_add_f32_e32 v73, v112, v73
	v_add_f32_e32 v74, v113, v74
	v_add_f32_e32 v75, v113, v75
	v_add_f32_e32 v76, v113, v76
	v_add_f32_e32 v77, v113, v77
	v_add_f32_e32 v78, v117, v78
	v_add_f32_e32 v79, v117, v79
	v_add_f32_e32 v80, v117, v80
	v_add_f32_e32 v81, v117, v81
	v_cvt_pk_f16_f32 v66, v66, v67
	v_cvt_pk_f16_f32 v67, v68, v69
	v_cvt_pk_f16_f32 v68, v70, v71
	v_cvt_pk_f16_f32 v69, v72, v73
	v_cvt_pk_f16_f32 v70, v74, v75
	v_cvt_pk_f16_f32 v71, v76, v77
	v_cvt_pk_f16_f32 v72, v78, v79
	v_cvt_pk_f16_f32 v73, v80, v81
	v_pk_max_f16 v66, v66, 0
	v_pk_max_f16 v67, v67, 0
	v_pk_max_f16 v68, v68, 0
	v_pk_max_f16 v69, v69, 0
	v_pk_max_f16 v70, v70, 0
	v_pk_max_f16 v71, v71, 0
	v_pk_max_f16 v72, v72, 0
	v_pk_max_f16 v73, v73, 0
	ds_write2_b64 v101, v[66:67], v[68:69] offset1:6
	ds_write2_b64 v101, v[70:71], v[72:73] offset0:12 offset1:18
	v_bfe_u32 v101, v99, 8, 8
	v_mad_u32_u24 v122, v115, 24, s7
	v_mad_u32_u24 v101, v101, s13, v122
	v_add_u32_e32 v122, 0x8d8, v123
	s_waitcnt lgkmcnt(4)
	v_mfma_f32_32x32x16_f16 v[66:81], v[82:85], v[108:111], 0
	ds_read_b64 v[108:109], v122
	ds_read_b64 v[110:111], v122 offset:8
	v_add_u32_e32 v122, 0x890, v123
	s_waitcnt lgkmcnt(2)
	v_mfma_f32_32x32x16_f16 v[66:81], v[86:89], v[124:127], v[66:81]
	ds_read_b64 v[124:125], v102 offset:176
	ds_read_b64 v[126:127], v102 offset:184
	s_waitcnt lgkmcnt(2)
	v_mfma_f32_32x32x16_f16 v[66:81], v[90:93], v[108:111], v[66:81]
	ds_read_b64 v[108:109], v122
	ds_read_b64 v[110:111], v122 offset:8
	s_waitcnt lgkmcnt(2)
	v_mfma_f32_32x32x16_f16 v[66:81], v[94:97], v[124:127], v[66:81]
	s_waitcnt lgkmcnt(0)
	v_mfma_f32_32x32x16_f16 v[66:81], v[118:121], v[108:111], v[66:81]
	v_bfe_u32 v124, v99, 16, 8
	v_mul_lo_u16_e32 v126, 0x4f, v124
	v_lshrrev_b16_e32 v126, 9, v126
	v_and_b32_e32 v126, 62, v126
	v_add_u32_e32 v126, v124, v126
	v_mov_b32_e32 v123, s8
	v_mad_u32_u24 v126, v126, s6, v123
	v_mad_u32_u24 v123, v115, s6, v126
	v_mad_u32_u24 v102, v115, s12, v126
	ds_read_b64 v[108:109], v123 offset:32
	ds_read_b64 v[110:111], v123 offset:40
	ds_read_b64 v[124:125], v123 offset:1112
	ds_read_b64 v[126:127], v123 offset:1120
	v_add_f32_e32 v66, v107, v66
	v_add_f32_e32 v67, v107, v67
	v_add_f32_e32 v68, v107, v68
	v_add_f32_e32 v69, v107, v69
	v_add_f32_e32 v70, v112, v70
	v_add_f32_e32 v71, v112, v71
	v_add_f32_e32 v72, v112, v72
	v_add_f32_e32 v73, v112, v73
	v_add_f32_e32 v74, v113, v74
	v_add_f32_e32 v75, v113, v75
	v_add_f32_e32 v76, v113, v76
	v_add_f32_e32 v77, v113, v77
	v_add_f32_e32 v78, v117, v78
	v_add_f32_e32 v79, v117, v79
	v_add_f32_e32 v80, v117, v80
	v_add_f32_e32 v81, v117, v81
	v_cvt_pk_f16_f32 v66, v66, v67
	v_cvt_pk_f16_f32 v67, v68, v69
	v_cvt_pk_f16_f32 v68, v70, v71
	v_cvt_pk_f16_f32 v69, v72, v73
	v_cvt_pk_f16_f32 v70, v74, v75
	v_cvt_pk_f16_f32 v71, v76, v77
	v_cvt_pk_f16_f32 v72, v78, v79
	v_cvt_pk_f16_f32 v73, v80, v81
	v_pk_max_f16 v66, v66, 0
	v_pk_max_f16 v67, v67, 0
	v_pk_max_f16 v68, v68, 0
	v_pk_max_f16 v69, v69, 0
	v_pk_max_f16 v70, v70, 0
	v_pk_max_f16 v71, v71, 0
	v_pk_max_f16 v72, v72, 0
	v_pk_max_f16 v73, v73, 0
	ds_write2_b64 v101, v[66:67], v[68:69] offset1:6
	ds_write2_b64 v101, v[70:71], v[72:73] offset0:12 offset1:18
	v_bfe_u32 v101, v99, 16, 8
	v_mad_u32_u24 v122, v115, 24, s7
	v_mad_u32_u24 v101, v101, s13, v122
	v_add_u32_e32 v122, 0x8d8, v123
	s_waitcnt lgkmcnt(4)
	v_mfma_f32_32x32x16_f16 v[66:81], v[82:85], v[108:111], 0
	ds_read_b64 v[108:109], v122
	ds_read_b64 v[110:111], v122 offset:8
	v_add_u32_e32 v122, 0x890, v123
	s_waitcnt lgkmcnt(2)
	v_mfma_f32_32x32x16_f16 v[66:81], v[86:89], v[124:127], v[66:81]
	ds_read_b64 v[124:125], v102 offset:176
	ds_read_b64 v[126:127], v102 offset:184
	s_waitcnt lgkmcnt(2)
	v_mfma_f32_32x32x16_f16 v[66:81], v[90:93], v[108:111], v[66:81]
	ds_read_b64 v[108:109], v122
	ds_read_b64 v[110:111], v122 offset:8
	s_waitcnt lgkmcnt(2)
	v_mfma_f32_32x32x16_f16 v[66:81], v[94:97], v[124:127], v[66:81]
	s_waitcnt lgkmcnt(0)
	v_mfma_f32_32x32x16_f16 v[66:81], v[118:121], v[108:111], v[66:81]
	v_or_b32_e32 v99, 32, v114
	v_or_b32_e32 v102, 64, v114
	s_nop 9
	v_add_f32_e32 v66, v107, v66
	v_add_f32_e32 v67, v107, v67
	v_add_f32_e32 v68, v107, v68
	v_add_f32_e32 v69, v107, v69
	v_add_f32_e32 v70, v112, v70
	v_add_f32_e32 v71, v112, v71
	v_add_f32_e32 v72, v112, v72
	v_add_f32_e32 v73, v112, v73
	v_add_f32_e32 v74, v113, v74
	v_add_f32_e32 v75, v113, v75
	v_add_f32_e32 v76, v113, v76
	v_add_f32_e32 v77, v113, v77
	v_add_f32_e32 v78, v117, v78
	v_add_f32_e32 v79, v117, v79
	v_add_f32_e32 v80, v117, v80
	v_add_f32_e32 v81, v117, v81
	v_cvt_pk_f16_f32 v66, v66, v67
	v_cvt_pk_f16_f32 v67, v68, v69
	v_cvt_pk_f16_f32 v68, v70, v71
	v_cvt_pk_f16_f32 v69, v72, v73
	v_cvt_pk_f16_f32 v70, v74, v75
	v_cvt_pk_f16_f32 v71, v76, v77
	v_cvt_pk_f16_f32 v72, v78, v79
	v_cvt_pk_f16_f32 v73, v80, v81
	v_pk_max_f16 v66, v66, 0
	v_pk_max_f16 v67, v67, 0
	v_pk_max_f16 v68, v68, 0
	v_pk_max_f16 v69, v69, 0
	v_pk_max_f16 v70, v70, 0
	v_pk_max_f16 v71, v71, 0
	v_pk_max_f16 v72, v72, 0
	v_pk_max_f16 v73, v73, 0
	ds_write2_b64 v101, v[66:67], v[68:69] offset1:6
	ds_write2_b64 v101, v[70:71], v[72:73] offset0:12 offset1:18
	v_or_b32_e32 v101, 0x60, v114
